# scatter output phase unrolled: LDS reads batched 5 edges at a time instead of two dependent LDS round trips per edge
# baseline (speedup 1.0000x reference)
.Lscat_out:
	v_add_u32_e32 v3, 0x9c40, v2
	v_cmp_gt_u32_e32 vcc, 0x310, v0
	s_mov_b32 s6, 0x186a0
	ds_read_u16 v20, v1 offset:0
	ds_read_b32 v30, v2 offset:0
	ds_read_b32 v31, v3 offset:0
	ds_read_u16 v21, v1 offset:2048
	ds_read_b32 v32, v2 offset:4096
	ds_read_b32 v33, v3 offset:4096
	ds_read_u16 v22, v1 offset:4096
	ds_read_b32 v34, v2 offset:8192
	ds_read_b32 v35, v3 offset:8192
	ds_read_u16 v23, v1 offset:6144
	ds_read_b32 v36, v2 offset:12288
	ds_read_b32 v37, v3 offset:12288
	ds_read_u16 v24, v1 offset:8192
	ds_read_b32 v38, v2 offset:16384
	ds_read_b32 v39, v3 offset:16384
	s_waitcnt lgkmcnt(0)
	v_lshl_add_u32 v20, v20, 2, s6
	ds_read_b32 v50, v20
	ds_read_b32 v60, v20 offset:16384
	v_lshl_add_u32 v21, v21, 2, s6
	ds_read_b32 v51, v21
	ds_read_b32 v61, v21 offset:16384
	v_lshl_add_u32 v22, v22, 2, s6
	ds_read_b32 v52, v22
	ds_read_b32 v62, v22 offset:16384
	v_lshl_add_u32 v23, v23, 2, s6
	ds_read_b32 v53, v23
	ds_read_b32 v63, v23 offset:16384
	v_lshl_add_u32 v24, v24, 2, s6
	ds_read_b32 v54, v24
	ds_read_b32 v64, v24 offset:16384
	s_waitcnt lgkmcnt(0)
	v_sub_u32_e32 v50, v50, v60
	v_add_u32_e32 v50, v0, v50
	v_lshlrev_b32_e32 v50, 3, v50
	global_store_dwordx2 v50, v[30:31], s[14:15]
	v_sub_u32_e32 v51, v51, v61
	v_add_u32_e32 v51, 0x400, v51
	v_add_u32_e32 v51, v0, v51
	v_lshlrev_b32_e32 v51, 3, v51
	global_store_dwordx2 v51, v[32:33], s[14:15]
	v_sub_u32_e32 v52, v52, v62
	v_add_u32_e32 v52, 0x800, v52
	v_add_u32_e32 v52, v0, v52
	v_lshlrev_b32_e32 v52, 3, v52
	global_store_dwordx2 v52, v[34:35], s[14:15]
	v_sub_u32_e32 v53, v53, v63
	v_add_u32_e32 v53, 0xc00, v53
	v_add_u32_e32 v53, v0, v53
	v_lshlrev_b32_e32 v53, 3, v53
	global_store_dwordx2 v53, v[36:37], s[14:15]
	v_sub_u32_e32 v54, v54, v64
	v_add_u32_e32 v54, 0x1000, v54
	v_add_u32_e32 v54, v0, v54
	v_lshlrev_b32_e32 v54, 3, v54
	global_store_dwordx2 v54, v[38:39], s[14:15]
	ds_read_u16 v25, v1 offset:10240
	ds_read_b32 v40, v2 offset:20480
	ds_read_b32 v41, v3 offset:20480
	ds_read_u16 v26, v1 offset:12288
	ds_read_b32 v42, v2 offset:24576
	ds_read_b32 v43, v3 offset:24576
	ds_read_u16 v27, v1 offset:14336
	ds_read_b32 v44, v2 offset:28672
	ds_read_b32 v45, v3 offset:28672
	ds_read_u16 v28, v1 offset:16384
	ds_read_b32 v46, v2 offset:32768
	ds_read_b32 v47, v3 offset:32768
	s_and_saveexec_b64 s[0:1], vcc
	ds_read_u16 v29, v1 offset:18432
	ds_read_b32 v48, v2 offset:36864
	ds_read_b32 v49, v3 offset:36864
	s_or_b64 exec, exec, s[0:1]
	s_waitcnt lgkmcnt(0)
	v_lshl_add_u32 v25, v25, 2, s6
	ds_read_b32 v55, v25
	ds_read_b32 v65, v25 offset:16384
	v_lshl_add_u32 v26, v26, 2, s6
	ds_read_b32 v56, v26
	ds_read_b32 v66, v26 offset:16384
	v_lshl_add_u32 v27, v27, 2, s6
	ds_read_b32 v57, v27
	ds_read_b32 v67, v27 offset:16384
	v_lshl_add_u32 v28, v28, 2, s6
	ds_read_b32 v58, v28
	ds_read_b32 v68, v28 offset:16384
	s_and_saveexec_b64 s[0:1], vcc
	v_lshl_add_u32 v29, v29, 2, s6
	ds_read_b32 v59, v29
	ds_read_b32 v69, v29 offset:16384
	s_or_b64 exec, exec, s[0:1]
	s_waitcnt lgkmcnt(0)
	v_sub_u32_e32 v55, v55, v65
	v_add_u32_e32 v55, 0x1400, v55
	v_add_u32_e32 v55, v0, v55
	v_lshlrev_b32_e32 v55, 3, v55
	global_store_dwordx2 v55, v[40:41], s[14:15]
	v_sub_u32_e32 v56, v56, v66
	v_add_u32_e32 v56, 0x1800, v56
	v_add_u32_e32 v56, v0, v56
	v_lshlrev_b32_e32 v56, 3, v56
	global_store_dwordx2 v56, v[42:43], s[14:15]
	v_sub_u32_e32 v57, v57, v67
	v_add_u32_e32 v57, 0x1c00, v57
	v_add_u32_e32 v57, v0, v57
	v_lshlrev_b32_e32 v57, 3, v57
	global_store_dwordx2 v57, v[44:45], s[14:15]
	v_sub_u32_e32 v58, v58, v68
	v_add_u32_e32 v58, 0x2000, v58
	v_add_u32_e32 v58, v0, v58
	v_lshlrev_b32_e32 v58, 3, v58
	global_store_dwordx2 v58, v[46:47], s[14:15]
	s_and_saveexec_b64 s[0:1], vcc
	v_sub_u32_e32 v59, v59, v69
	v_add_u32_e32 v59, 0x2400, v59
	v_add_u32_e32 v59, v0, v59
	v_lshlrev_b32_e32 v59, 3, v59
	global_store_dwordx2 v59, v[48:49], s[14:15]
	s_or_b64 exec, exec, s[0:1]
	s_endpgm
